# prologue: waves 4-7 staggered by s_sleep 10 behind waves 0-3 so same-program LDS waits interleave
# speedup vs baseline: 1.0078x; 1.0078x over previous
.LBB0_5:
	s_or_b64 exec, exec, s[4:5]
	s_lshr_b32 s33, s3, 6
	s_lshl_b32 s3, s33, 7
	v_bfe_u32 v70, v0, 4, 2
	s_lshl_b32 s4, s2, 2
	v_or_b32_e32 v18, s3, v70
	v_lshlrev_b32_e32 v2, 4, v0
	s_and_b32 s25, s4, 28
	v_and_b32_e32 v84, 0xf0, v2
	v_or_b32_e32 v2, s25, v18
	s_add_i32 s5, s4, 4
	v_lshl_or_b32 v2, v2, 8, v84
	s_and_b32 s34, s5, 28
	s_waitcnt lgkmcnt(0)
	global_load_dwordx4 v[2:5], v2, s[22:23]
	v_or_b32_e32 v6, s34, v18
	s_add_i32 s5, s4, 8
	v_lshl_or_b32 v6, v6, 8, v84
	s_and_b32 s35, s5, 28
	global_load_dwordx4 v[6:9], v6, s[22:23]
	v_or_b32_e32 v10, s35, v18
	s_add_i32 s5, s4, 12
	v_lshl_or_b32 v10, v10, 8, v84
	s_and_b32 s36, s5, 28
	global_load_dwordx4 v[10:13], v10, s[22:23]
	v_or_b32_e32 v14, s36, v18
	v_lshl_or_b32 v14, v14, 8, v84
	s_xor_b32 s37, s25, 16
	global_load_dwordx4 v[14:17], v14, s[22:23]
	v_or_b32_e32 v19, s37, v18
	s_add_i32 s5, s4, 20
	v_lshl_or_b32 v19, v19, 8, v84
	s_and_b32 s38, s5, 28
	global_load_dwordx4 v[46:49], v19, s[22:23]
	v_or_b32_e32 v20, s38, v18
	s_add_i32 s7, s4, 24
	v_lshl_or_b32 v20, v20, 8, v84
	s_and_b32 s39, s7, 28
	global_load_dwordx4 v[50:53], v20, s[22:23]
	v_or_b32_e32 v20, s39, v18
	s_add_i32 s4, s4, 28
	v_lshl_or_b32 v20, v20, 8, v84
	s_and_b32 s40, s4, 28
	global_load_dwordx4 v[58:61], v20, s[22:23]
	v_or_b32_e32 v18, s40, v18
	v_lshl_or_b32 v18, v18, 8, v84
	global_load_dwordx4 v[62:65], v18, s[22:23]
	v_lshlrev_b32_e32 v19, 3, v0
	s_mul_i32 s6, s33, 0x1200
	v_and_b32_e32 v19, 0x78, v19
	v_or_b32_e32 v85, 32, v70
	v_or_b32_e32 v93, s6, v19
	v_or_b32_e32 v19, s3, v85
	v_bfe_u32 v184, v0, 5, 1
	v_and_b32_e32 v181, 31, v0
	s_movk_i32 s5, 0x90
	v_mov_b32_e32 v18, s6
	v_or_b32_e32 v20, s25, v19
	v_lshlrev_b32_e32 v182, 4, v184
	v_mad_u32_u24 v18, v181, s5, v18
	v_or_b32_e32 v21, s34, v19
	v_or_b32_e32 v22, s35, v19
	v_or_b32_e32 v23, s36, v19
	v_or_b32_e32 v24, s37, v19
	v_or_b32_e32 v25, s38, v19
	v_or_b32_e32 v26, s39, v19
	v_or_b32_e32 v19, s40, v19
	v_lshl_or_b32 v43, v20, 8, v84
	v_add_u32_e32 v82, v18, v182
	v_lshl_or_b32 v44, v21, 8, v84
	v_lshl_or_b32 v45, v22, 8, v84
	v_lshl_or_b32 v71, v23, 8, v84
	v_lshl_or_b32 v72, v24, 8, v84
	v_lshl_or_b32 v73, v25, 8, v84
	v_lshl_or_b32 v74, v26, 8, v84
	v_lshl_or_b32 v75, v19, 8, v84
	global_load_dwordx4 v[66:69], v43, s[22:23]
	global_load_dwordx4 v[54:57], v44, s[22:23]
	global_load_dwordx4 v[38:41], v45, s[22:23]
	global_load_dwordx4 v[34:37], v71, s[22:23]
	global_load_dwordx4 v[30:33], v72, s[22:23]
	global_load_dwordx4 v[26:29], v73, s[22:23]
	global_load_dwordx4 v[22:25], v74, s[22:23]
	global_load_dwordx4 v[18:21], v75, s[22:23]
	v_or_b32_e32 v42, s25, v70
	v_or_b32_e32 v43, s34, v70
	v_or_b32_e32 v44, s35, v70
	v_or_b32_e32 v45, s36, v70
	s_waitcnt vmcnt(15)
	s_cmp_lt_u32 s33, 4
	s_cbranch_scc1 .Lno_stagger
	s_sleep 10
.Lno_stagger:
	v_cvt_pk_f16_f32 v2, -v2, -v3
	v_cvt_pk_f16_f32 v3, -v4, -v5
	v_mad_u32_u24 v4, v42, s5, v93
	ds_write_b64 v4, v[2:3]
	s_waitcnt vmcnt(14)
	v_cvt_pk_f16_f32 v2, -v6, -v7
	v_cvt_pk_f16_f32 v3, -v8, -v9
	v_mad_u32_u24 v4, v43, s5, v93
	ds_write_b64 v4, v[2:3]
	s_waitcnt vmcnt(13)
	v_cvt_pk_f16_f32 v2, -v10, -v11
	v_cvt_pk_f16_f32 v3, -v12, -v13
	v_mad_u32_u24 v4, v44, s5, v93
	ds_write_b64 v4, v[2:3]
	s_waitcnt vmcnt(12)
	v_cvt_pk_f16_f32 v2, -v14, -v15
	v_cvt_pk_f16_f32 v3, -v16, -v17
	v_mad_u32_u24 v4, v45, s5, v93
	ds_write_b64 v4, v[2:3]
	s_waitcnt vmcnt(11)
	v_cvt_pk_f16_f32 v2, -v46, -v47
	v_cvt_pk_f16_f32 v3, -v48, -v49
	v_bitop3_b32 v46, s25, v70, 16 bitop3:0xde
	v_mad_u32_u24 v4, v46, s5, v93
	ds_write_b64 v4, v[2:3]
	s_waitcnt vmcnt(10)
	v_cvt_pk_f16_f32 v2, -v50, -v51
	v_cvt_pk_f16_f32 v3, -v52, -v53
	v_or_b32_e32 v47, s38, v70
	v_mad_u32_u24 v4, v47, s5, v93
	ds_write_b64 v4, v[2:3]
	s_waitcnt vmcnt(9)
	v_cvt_pk_f16_f32 v2, -v58, -v59
	v_cvt_pk_f16_f32 v3, -v60, -v61
	v_or_b32_e32 v48, s39, v70
	v_mad_u32_u24 v4, v48, s5, v93
	ds_write_b64 v4, v[2:3]
	s_waitcnt vmcnt(8)
	v_cvt_pk_f16_f32 v2, -v62, -v63
	v_cvt_pk_f16_f32 v3, -v64, -v65
	v_or_b32_e32 v49, s40, v70
	v_mad_u32_u24 v4, v49, s5, v93
	ds_write_b64 v4, v[2:3]
	s_waitcnt lgkmcnt(0)
	ds_read_b128 v[98:101], v82
	ds_read_b128 v[102:105], v82 offset:32
	s_waitcnt lgkmcnt(1)
	v_mfma_f32_32x32x16_f16 v[2:17], v[98:101], v[98:101], 0
	ds_read_b128 v[106:109], v82 offset:64
	ds_read_b128 v[110:113], v82 offset:96
	s_waitcnt lgkmcnt(0)
	v_and_b32_e32 v50, 3, v0
	v_cmp_ne_u32_e64 s[6:7], 0, v50
	v_cmp_ne_u32_e64 s[4:5], 1, v50
	v_cmp_eq_u32_e32 vcc, 2, v50
	s_waitcnt lgkmcnt(2)
	v_mfma_f32_32x32x16_f16 v[2:17], v[102:105], v[102:105], v[2:17]
	s_waitcnt lgkmcnt(1)
	v_mfma_f32_32x32x16_f16 v[2:17], v[106:109], v[106:109], v[2:17]
	s_waitcnt lgkmcnt(0)
	v_mfma_f32_32x32x16_f16 v[2:17], v[110:113], v[110:113], v[2:17]
	s_and_saveexec_b64 s[8:9], s[6:7]
	s_xor_b64 s[8:9], exec, s[8:9]
	s_cbranch_execz .LBB0_9
	s_nop 8
	v_mov_b32_e32 v2, v3
	s_and_saveexec_b64 s[12:13], s[4:5]
	s_xor_b64 s[12:13], exec, s[12:13]
	v_cndmask_b32_e32 v2, v5, v4, vcc
	s_andn2_saveexec_b64 s[12:13], s[12:13]
	s_or_b64 exec, exec, s[12:13]
